# moe1 SwiGLU epilogue rewritten: packed f32 ops on accumulator pairs, constants folded into exp arg and rcp input (bit-identical association)
# speedup vs baseline: 1.0214x; 1.0075x over previous
; #define GAS __attribute__((address_space(1)))
; __device__ __forceinline__ float sigmoidf_(float x) { return __builtin_amdgcn_rcpf(1.0f + __expf(-x)); }
;     __device__ __forceinline__ void operator()(const f32x4 (&acc)[2][2][4][2], const Unit& u, int wr, int wc, int fr, int fq) const {
;     ...
;             for (int mp = 0; mp < 4; mp += 2) { v2u wq[2];
; #pragma unroll
;                 for (int q = 0; q < 2; ++q) { const int m = mp + q;
;                     const f32x4 g0 = acc[ai][0][m][0] * sg, g1 = acc[ai][0][m][1] * sg, u0 = acc[ai][1][m][0] * (sg * FP8_SA), u1 = acc[ai][1][m][1] * (sg * FP8_SA);
;                     float r[8];
; #pragma unroll
;                     for (int j = 0; j < 4; ++j) { r[j] = g0[j] * sigmoidf_(g0[j]) * u0[j]; r[4 + j] = g1[j] * sigmoidf_(g1[j]) * u1[j]; }
;                     wq[q].x = pk4_fp8(r[0], r[1], r[2], r[3]); wq[q].y = pk4_fp8(r[4], r[5], r[6], r[7]); }
;                 const auto sx = __builtin_amdgcn_permlane16_swap(wq[0].x, wq[1].x, false, false), sy = __builtin_amdgcn_permlane16_swap(wq[0].y, wq[1].y, false, false);
;                 v4u w; w.x = sx[0]; w.y = sy[0]; w.z = sx[1]; w.w = sy[1];
;                 const int odd = fq & 1;
;                 *(GAS v4u*)(act + (size_t)(row0 + ai * 128 + (mp + odd) * 16) * DF + f0 - 8 * odd) = w; }
.LBB0_1086:
	s_mov_b32 s98, 0xbab8aa3b
	s_mov_b32 s99, 0xbab8aa3b
	s_mov_b32 s100, 0x48000000
	s_mov_b32 s101, 0x48000000
	v_lshl_add_u32 v4, s71, 8, v240
	v_lshl_or_b32 v2, s28, 7, v244
	v_add_u32_e32 v5, 0x80, v4
	v_ashrrev_i32_e32 v3, 31, v2
	v_pk_mul_f32 v[12:13], v[190:191], s[98:99]
	v_pk_mul_f32 v[14:15], v[192:193], s[98:99]
	v_pk_mul_f32 v[16:17], v[186:187], s[98:99]
	v_pk_mul_f32 v[18:19], v[188:189], s[98:99]
	v_exp_f32_e32 v12, v12
	v_exp_f32_e32 v13, v13
	v_exp_f32_e32 v14, v14
	v_exp_f32_e32 v15, v15
	v_exp_f32_e32 v16, v16
	v_exp_f32_e32 v17, v17
	v_exp_f32_e32 v18, v18
	v_exp_f32_e32 v19, v19
	v_pk_fma_f32 v[12:13], v[12:13], s[100:101], s[100:101]
	v_pk_fma_f32 v[14:15], v[14:15], s[100:101], s[100:101]
	v_pk_fma_f32 v[16:17], v[16:17], s[100:101], s[100:101]
	v_pk_fma_f32 v[18:19], v[18:19], s[100:101], s[100:101]
	v_rcp_f32_e32 v12, v12
	v_rcp_f32_e32 v13, v13
	v_rcp_f32_e32 v14, v14
	v_rcp_f32_e32 v15, v15
	v_rcp_f32_e32 v16, v16
	v_rcp_f32_e32 v17, v17
	v_rcp_f32_e32 v18, v18
	v_rcp_f32_e32 v19, v19
	v_pk_mul_f32 v[12:13], v[190:191], v[12:13]
	v_pk_mul_f32 v[14:15], v[192:193], v[14:15]
	v_pk_mul_f32 v[16:17], v[186:187], v[16:17]
	v_pk_mul_f32 v[18:19], v[188:189], v[18:19]
	v_pk_mul_f32 v[12:13], v[12:13], v[158:159]
	v_pk_mul_f32 v[14:15], v[14:15], v[160:161]
	v_pk_mul_f32 v[16:17], v[16:17], v[154:155]
	v_pk_mul_f32 v[18:19], v[18:19], v[156:157]
	v_med3_f32 v12, v12, s69, v246
	v_med3_f32 v13, v13, s69, v246
	v_med3_f32 v14, v14, s69, v246
	v_med3_f32 v15, v15, s69, v246
	v_med3_f32 v16, v16, s69, v246
	v_med3_f32 v17, v17, s69, v246
	v_med3_f32 v18, v18, s69, v246
	v_med3_f32 v19, v19, s69, v246
	v_cvt_pk_fp8_f32 v6, v12, v13
	v_cvt_pk_fp8_f32 v7, v16, v17
	v_cvt_pk_fp8_f32 v6, v14, v15 op_sel:[0,0,1]
	v_cvt_pk_fp8_f32 v7, v18, v19 op_sel:[0,0,1]
	v_pk_mul_f32 v[20:21], v[182:183], s[98:99]
	v_pk_mul_f32 v[22:23], v[184:185], s[98:99]
	v_pk_mul_f32 v[24:25], v[178:179], s[98:99]
	v_pk_mul_f32 v[26:27], v[180:181], s[98:99]
	v_exp_f32_e32 v20, v20
	v_exp_f32_e32 v21, v21
	v_exp_f32_e32 v22, v22
	v_exp_f32_e32 v23, v23
	v_exp_f32_e32 v24, v24
	v_exp_f32_e32 v25, v25
	v_exp_f32_e32 v26, v26
	v_exp_f32_e32 v27, v27
	v_pk_fma_f32 v[20:21], v[20:21], s[100:101], s[100:101]
	v_pk_fma_f32 v[22:23], v[22:23], s[100:101], s[100:101]
	v_pk_fma_f32 v[24:25], v[24:25], s[100:101], s[100:101]
	v_pk_fma_f32 v[26:27], v[26:27], s[100:101], s[100:101]
	v_rcp_f32_e32 v20, v20
	v_rcp_f32_e32 v21, v21
	v_rcp_f32_e32 v22, v22
	v_rcp_f32_e32 v23, v23
	v_rcp_f32_e32 v24, v24
	v_rcp_f32_e32 v25, v25
	v_rcp_f32_e32 v26, v26
	v_rcp_f32_e32 v27, v27
	v_pk_mul_f32 v[20:21], v[182:183], v[20:21]
	v_pk_mul_f32 v[22:23], v[184:185], v[22:23]
	v_pk_mul_f32 v[24:25], v[178:179], v[24:25]
	v_pk_mul_f32 v[26:27], v[180:181], v[26:27]
	v_pk_mul_f32 v[20:21], v[20:21], v[150:151]
	v_pk_mul_f32 v[22:23], v[22:23], v[152:153]
	v_pk_mul_f32 v[24:25], v[24:25], v[146:147]
	v_pk_mul_f32 v[26:27], v[26:27], v[148:149]
	v_med3_f32 v20, v20, s69, v246
	v_med3_f32 v21, v21, s69, v246
	v_med3_f32 v22, v22, s69, v246
	v_med3_f32 v23, v23, s69, v246
	v_med3_f32 v24, v24, s69, v246
	v_med3_f32 v25, v25, s69, v246
	v_med3_f32 v26, v26, s69, v246
	v_med3_f32 v27, v27, s69, v246
	v_cvt_pk_fp8_f32 v8, v20, v21
	v_cvt_pk_fp8_f32 v9, v24, v25
	v_cvt_pk_fp8_f32 v8, v22, v23 op_sel:[0,0,1]
	v_cvt_pk_fp8_f32 v9, v26, v27 op_sel:[0,0,1]
	v_or_b32_e32 v10, v4, v242
	v_ashrrev_i32_e32 v11, 31, v10
	v_lshlrev_b64 v[10:11], 11, v[10:11]
	v_lshl_add_u64 v[10:11], s[8:9], 0, v[10:11]
	v_lshl_add_u64 v[10:11], v[10:11], 0, v[2:3]
	v_permlane16_swap_b32_e32 v6, v8
	v_permlane16_swap_b32_e32 v7, v9
	v_lshl_add_u64 v[10:11], v[10:11], 0, v[210:211]
	global_store_dwordx4 v[10:11], v[6:9], off
	s_nop 1
	v_pk_mul_f32 v[12:13], v[174:175], s[98:99]
	v_pk_mul_f32 v[14:15], v[176:177], s[98:99]
	v_pk_mul_f32 v[16:17], v[170:171], s[98:99]
	v_pk_mul_f32 v[18:19], v[172:173], s[98:99]
	v_exp_f32_e32 v12, v12
	v_exp_f32_e32 v13, v13
	v_exp_f32_e32 v14, v14
	v_exp_f32_e32 v15, v15
	v_exp_f32_e32 v16, v16
	v_exp_f32_e32 v17, v17
	v_exp_f32_e32 v18, v18
	v_exp_f32_e32 v19, v19
	v_pk_fma_f32 v[12:13], v[12:13], s[100:101], s[100:101]
	v_pk_fma_f32 v[14:15], v[14:15], s[100:101], s[100:101]
	v_pk_fma_f32 v[16:17], v[16:17], s[100:101], s[100:101]
	v_pk_fma_f32 v[18:19], v[18:19], s[100:101], s[100:101]
	v_rcp_f32_e32 v12, v12
	v_rcp_f32_e32 v13, v13
	v_rcp_f32_e32 v14, v14
	v_rcp_f32_e32 v15, v15
	v_rcp_f32_e32 v16, v16
	v_rcp_f32_e32 v17, v17
	v_rcp_f32_e32 v18, v18
	v_rcp_f32_e32 v19, v19
	v_pk_mul_f32 v[12:13], v[174:175], v[12:13]
	v_pk_mul_f32 v[14:15], v[176:177], v[14:15]
	v_pk_mul_f32 v[16:17], v[170:171], v[16:17]
	v_pk_mul_f32 v[18:19], v[172:173], v[18:19]
	v_pk_mul_f32 v[12:13], v[12:13], v[142:143]
	v_pk_mul_f32 v[14:15], v[14:15], v[144:145]
	v_pk_mul_f32 v[16:17], v[16:17], v[138:139]
	v_pk_mul_f32 v[18:19], v[18:19], v[140:141]
	v_med3_f32 v12, v12, s69, v246
	v_med3_f32 v13, v13, s69, v246
	v_med3_f32 v14, v14, s69, v246
	v_med3_f32 v15, v15, s69, v246
	v_med3_f32 v16, v16, s69, v246
	v_med3_f32 v17, v17, s69, v246
	v_med3_f32 v18, v18, s69, v246
	v_med3_f32 v19, v19, s69, v246
	v_cvt_pk_fp8_f32 v6, v12, v13
	v_cvt_pk_fp8_f32 v7, v16, v17
	v_cvt_pk_fp8_f32 v6, v14, v15 op_sel:[0,0,1]
	v_cvt_pk_fp8_f32 v7, v18, v19 op_sel:[0,0,1]
	v_pk_mul_f32 v[20:21], v[166:167], s[98:99]
	v_pk_mul_f32 v[22:23], v[168:169], s[98:99]
	v_pk_mul_f32 v[24:25], v[162:163], s[98:99]
	v_pk_mul_f32 v[26:27], v[164:165], s[98:99]
	v_exp_f32_e32 v20, v20
	v_exp_f32_e32 v21, v21
	v_exp_f32_e32 v22, v22
	v_exp_f32_e32 v23, v23
	v_exp_f32_e32 v24, v24
	v_exp_f32_e32 v25, v25
	v_exp_f32_e32 v26, v26
; #define GAS __attribute__((address_space(1)))
; __device__ __forceinline__ float sigmoidf_(float x) { return __builtin_amdgcn_rcpf(1.0f + __expf(-x)); }
;     __device__ __forceinline__ void operator()(const f32x4 (&acc)[2][2][4][2], const Unit& u, int wr, int wc, int fr, int fq) const {
;     ...
;             for (int mp = 0; mp < 4; mp += 2) { v2u wq[2];
; #pragma unroll
;                 for (int q = 0; q < 2; ++q) { const int m = mp + q;
;                     const f32x4 g0 = acc[ai][0][m][0] * sg, g1 = acc[ai][0][m][1] * sg, u0 = acc[ai][1][m][0] * (sg * FP8_SA), u1 = acc[ai][1][m][1] * (sg * FP8_SA);
;                     float r[8];
; #pragma unroll
;                     for (int j = 0; j < 4; ++j) { r[j] = g0[j] * sigmoidf_(g0[j]) * u0[j]; r[4 + j] = g1[j] * sigmoidf_(g1[j]) * u1[j]; }
;                     wq[q].x = pk4_fp8(r[0], r[1], r[2], r[3]); wq[q].y = pk4_fp8(r[4], r[5], r[6], r[7]); }
;                 const auto sx = __builtin_amdgcn_permlane16_swap(wq[0].x, wq[1].x, false, false), sy = __builtin_amdgcn_permlane16_swap(wq[0].y, wq[1].y, false, false);
;                 v4u w; w.x = sx[0]; w.y = sy[0]; w.z = sx[1]; w.w = sy[1];
;                 const int odd = fq & 1;
;                 *(GAS v4u*)(act + (size_t)(row0 + ai * 128 + (mp + odd) * 16) * DF + f0 - 8 * odd) = w; }
	v_exp_f32_e32 v27, v27
	v_pk_fma_f32 v[20:21], v[20:21], s[100:101], s[100:101]
	v_pk_fma_f32 v[22:23], v[22:23], s[100:101], s[100:101]
	v_pk_fma_f32 v[24:25], v[24:25], s[100:101], s[100:101]
	v_pk_fma_f32 v[26:27], v[26:27], s[100:101], s[100:101]
	v_rcp_f32_e32 v20, v20
	v_rcp_f32_e32 v21, v21
	v_rcp_f32_e32 v22, v22
	v_rcp_f32_e32 v23, v23
	v_rcp_f32_e32 v24, v24
	v_rcp_f32_e32 v25, v25
	v_rcp_f32_e32 v26, v26
	v_rcp_f32_e32 v27, v27
	v_pk_mul_f32 v[20:21], v[166:167], v[20:21]
	v_pk_mul_f32 v[22:23], v[168:169], v[22:23]
	v_pk_mul_f32 v[24:25], v[162:163], v[24:25]
	v_pk_mul_f32 v[26:27], v[164:165], v[26:27]
	v_pk_mul_f32 v[20:21], v[20:21], v[134:135]
	v_pk_mul_f32 v[22:23], v[22:23], v[136:137]
	v_pk_mul_f32 v[24:25], v[24:25], v[130:131]
	v_pk_mul_f32 v[26:27], v[26:27], v[132:133]
	v_med3_f32 v20, v20, s69, v246
	v_med3_f32 v21, v21, s69, v246
	v_med3_f32 v22, v22, s69, v246
	v_med3_f32 v23, v23, s69, v246
	v_med3_f32 v24, v24, s69, v246
	v_med3_f32 v25, v25, s69, v246
	v_med3_f32 v26, v26, s69, v246
	v_med3_f32 v27, v27, s69, v246
	v_cvt_pk_fp8_f32 v8, v20, v21
	v_cvt_pk_fp8_f32 v9, v24, v25
	v_cvt_pk_fp8_f32 v8, v22, v23 op_sel:[0,0,1]
	v_cvt_pk_fp8_f32 v9, v26, v27 op_sel:[0,0,1]
	v_or_b32_e32 v10, v4, v243
	v_ashrrev_i32_e32 v11, 31, v10
	v_lshlrev_b64 v[10:11], 11, v[10:11]
	v_lshl_add_u64 v[10:11], s[8:9], 0, v[10:11]
	v_lshl_add_u64 v[10:11], v[10:11], 0, v[2:3]
	v_permlane16_swap_b32_e32 v6, v8
	v_permlane16_swap_b32_e32 v7, v9
	v_lshl_add_u64 v[10:11], v[10:11], 0, v[210:211]
	global_store_dwordx4 v[10:11], v[6:9], off
	s_nop 1
	v_pk_mul_f32 v[12:13], v[126:127], s[98:99]
	v_pk_mul_f32 v[14:15], v[128:129], s[98:99]
	v_pk_mul_f32 v[16:17], v[122:123], s[98:99]
	v_pk_mul_f32 v[18:19], v[124:125], s[98:99]
	v_exp_f32_e32 v12, v12
	v_exp_f32_e32 v13, v13
	v_exp_f32_e32 v14, v14
	v_exp_f32_e32 v15, v15
	v_exp_f32_e32 v16, v16
	v_exp_f32_e32 v17, v17
	v_exp_f32_e32 v18, v18
	v_exp_f32_e32 v19, v19
	v_pk_fma_f32 v[12:13], v[12:13], s[100:101], s[100:101]
	v_pk_fma_f32 v[14:15], v[14:15], s[100:101], s[100:101]
	v_pk_fma_f32 v[16:17], v[16:17], s[100:101], s[100:101]
	v_pk_fma_f32 v[18:19], v[18:19], s[100:101], s[100:101]
	v_rcp_f32_e32 v12, v12
	v_rcp_f32_e32 v13, v13
	v_rcp_f32_e32 v14, v14
	v_rcp_f32_e32 v15, v15
	v_rcp_f32_e32 v16, v16
	v_rcp_f32_e32 v17, v17
	v_rcp_f32_e32 v18, v18
	v_rcp_f32_e32 v19, v19
	v_pk_mul_f32 v[12:13], v[126:127], v[12:13]
	v_pk_mul_f32 v[14:15], v[128:129], v[14:15]
	v_pk_mul_f32 v[16:17], v[122:123], v[16:17]
	v_pk_mul_f32 v[18:19], v[124:125], v[18:19]
	v_pk_mul_f32 v[12:13], v[12:13], v[94:95]
	v_pk_mul_f32 v[14:15], v[14:15], v[96:97]
	v_pk_mul_f32 v[16:17], v[16:17], v[90:91]
	v_pk_mul_f32 v[18:19], v[18:19], v[92:93]
	v_med3_f32 v12, v12, s69, v246
	v_med3_f32 v13, v13, s69, v246
	v_med3_f32 v14, v14, s69, v246
	v_med3_f32 v15, v15, s69, v246
	v_med3_f32 v16, v16, s69, v246
	v_med3_f32 v17, v17, s69, v246
	v_med3_f32 v18, v18, s69, v246
	v_med3_f32 v19, v19, s69, v246
	v_cvt_pk_fp8_f32 v6, v12, v13
	v_cvt_pk_fp8_f32 v7, v16, v17
	v_cvt_pk_fp8_f32 v6, v14, v15 op_sel:[0,0,1]
	v_cvt_pk_fp8_f32 v7, v18, v19 op_sel:[0,0,1]
	v_pk_mul_f32 v[20:21], v[118:119], s[98:99]
	v_pk_mul_f32 v[22:23], v[120:121], s[98:99]
	v_pk_mul_f32 v[24:25], v[114:115], s[98:99]
	v_pk_mul_f32 v[26:27], v[116:117], s[98:99]
	v_exp_f32_e32 v20, v20
	v_exp_f32_e32 v21, v21
	v_exp_f32_e32 v22, v22
	v_exp_f32_e32 v23, v23
	v_exp_f32_e32 v24, v24
	v_exp_f32_e32 v25, v25
	v_exp_f32_e32 v26, v26
	v_exp_f32_e32 v27, v27
	v_pk_fma_f32 v[20:21], v[20:21], s[100:101], s[100:101]
	v_pk_fma_f32 v[22:23], v[22:23], s[100:101], s[100:101]
	v_pk_fma_f32 v[24:25], v[24:25], s[100:101], s[100:101]
	v_pk_fma_f32 v[26:27], v[26:27], s[100:101], s[100:101]
	v_rcp_f32_e32 v20, v20
	v_rcp_f32_e32 v21, v21
	v_rcp_f32_e32 v22, v22
	v_rcp_f32_e32 v23, v23
	v_rcp_f32_e32 v24, v24
	v_rcp_f32_e32 v25, v25
	v_rcp_f32_e32 v26, v26
	v_rcp_f32_e32 v27, v27
	v_pk_mul_f32 v[20:21], v[118:119], v[20:21]
	v_pk_mul_f32 v[22:23], v[120:121], v[22:23]
	v_pk_mul_f32 v[24:25], v[114:115], v[24:25]
	v_pk_mul_f32 v[26:27], v[116:117], v[26:27]
	v_pk_mul_f32 v[20:21], v[20:21], v[86:87]
	v_pk_mul_f32 v[22:23], v[22:23], v[88:89]
	v_pk_mul_f32 v[24:25], v[24:25], v[82:83]
	v_pk_mul_f32 v[26:27], v[26:27], v[84:85]
	v_med3_f32 v20, v20, s69, v246
	v_med3_f32 v21, v21, s69, v246
; #define GAS __attribute__((address_space(1)))
; __device__ __forceinline__ float sigmoidf_(float x) { return __builtin_amdgcn_rcpf(1.0f + __expf(-x)); }
;     __device__ __forceinline__ void operator()(const f32x4 (&acc)[2][2][4][2], const Unit& u, int wr, int wc, int fr, int fq) const {
;     ...
;             for (int mp = 0; mp < 4; mp += 2) { v2u wq[2];
; #pragma unroll
;                 for (int q = 0; q < 2; ++q) { const int m = mp + q;
;                     const f32x4 g0 = acc[ai][0][m][0] * sg, g1 = acc[ai][0][m][1] * sg, u0 = acc[ai][1][m][0] * (sg * FP8_SA), u1 = acc[ai][1][m][1] * (sg * FP8_SA);
;                     float r[8];
; #pragma unroll
;                     for (int j = 0; j < 4; ++j) { r[j] = g0[j] * sigmoidf_(g0[j]) * u0[j]; r[4 + j] = g1[j] * sigmoidf_(g1[j]) * u1[j]; }
;                     wq[q].x = pk4_fp8(r[0], r[1], r[2], r[3]); wq[q].y = pk4_fp8(r[4], r[5], r[6], r[7]); }
;                 const auto sx = __builtin_amdgcn_permlane16_swap(wq[0].x, wq[1].x, false, false), sy = __builtin_amdgcn_permlane16_swap(wq[0].y, wq[1].y, false, false);
;                 v4u w; w.x = sx[0]; w.y = sy[0]; w.z = sx[1]; w.w = sy[1];
;                 const int odd = fq & 1;
;                 *(GAS v4u*)(act + (size_t)(row0 + ai * 128 + (mp + odd) * 16) * DF + f0 - 8 * odd) = w; }
	v_med3_f32 v22, v22, s69, v246
	v_med3_f32 v23, v23, s69, v246
	v_med3_f32 v24, v24, s69, v246
	v_med3_f32 v25, v25, s69, v246
	v_med3_f32 v26, v26, s69, v246
	v_med3_f32 v27, v27, s69, v246
	v_cvt_pk_fp8_f32 v8, v20, v21
	v_cvt_pk_fp8_f32 v9, v24, v25
	v_cvt_pk_fp8_f32 v8, v22, v23 op_sel:[0,0,1]
	v_cvt_pk_fp8_f32 v9, v26, v27 op_sel:[0,0,1]
	v_or_b32_e32 v10, v5, v242
	v_ashrrev_i32_e32 v11, 31, v10
	v_lshlrev_b64 v[10:11], 11, v[10:11]
	v_lshl_add_u64 v[10:11], s[8:9], 0, v[10:11]
	v_lshl_add_u64 v[10:11], v[10:11], 0, v[2:3]
	v_permlane16_swap_b32_e32 v6, v8
	v_permlane16_swap_b32_e32 v7, v9
	v_lshl_add_u64 v[10:11], v[10:11], 0, v[210:211]
	global_store_dwordx4 v[10:11], v[6:9], off
	s_nop 1
	v_pk_mul_f32 v[12:13], v[110:111], s[98:99]
	v_pk_mul_f32 v[14:15], v[112:113], s[98:99]
	v_pk_mul_f32 v[16:17], v[106:107], s[98:99]
	v_pk_mul_f32 v[18:19], v[108:109], s[98:99]
	v_exp_f32_e32 v12, v12
	v_exp_f32_e32 v13, v13
	v_exp_f32_e32 v14, v14
	v_exp_f32_e32 v15, v15
	v_exp_f32_e32 v16, v16
	v_exp_f32_e32 v17, v17
	v_exp_f32_e32 v18, v18
	v_exp_f32_e32 v19, v19
	v_pk_fma_f32 v[12:13], v[12:13], s[100:101], s[100:101]
	v_pk_fma_f32 v[14:15], v[14:15], s[100:101], s[100:101]
	v_pk_fma_f32 v[16:17], v[16:17], s[100:101], s[100:101]
	v_pk_fma_f32 v[18:19], v[18:19], s[100:101], s[100:101]
	v_rcp_f32_e32 v12, v12
	v_rcp_f32_e32 v13, v13
	v_rcp_f32_e32 v14, v14
	v_rcp_f32_e32 v15, v15
	v_rcp_f32_e32 v16, v16
	v_rcp_f32_e32 v17, v17
	v_rcp_f32_e32 v18, v18
	v_rcp_f32_e32 v19, v19
	v_pk_mul_f32 v[12:13], v[110:111], v[12:13]
	v_pk_mul_f32 v[14:15], v[112:113], v[14:15]
	v_pk_mul_f32 v[16:17], v[106:107], v[16:17]
	v_pk_mul_f32 v[18:19], v[108:109], v[18:19]
	v_pk_mul_f32 v[12:13], v[12:13], v[78:79]
	v_pk_mul_f32 v[14:15], v[14:15], v[80:81]
	v_pk_mul_f32 v[16:17], v[16:17], v[74:75]
	v_pk_mul_f32 v[18:19], v[18:19], v[76:77]
	v_med3_f32 v12, v12, s69, v246
	v_med3_f32 v13, v13, s69, v246
	v_med3_f32 v14, v14, s69, v246
	v_med3_f32 v15, v15, s69, v246
	v_med3_f32 v16, v16, s69, v246
	v_med3_f32 v17, v17, s69, v246
	v_med3_f32 v18, v18, s69, v246
	v_med3_f32 v19, v19, s69, v246
	v_cvt_pk_fp8_f32 v6, v12, v13
	v_cvt_pk_fp8_f32 v7, v16, v17
	v_cvt_pk_fp8_f32 v6, v14, v15 op_sel:[0,0,1]
	v_cvt_pk_fp8_f32 v7, v18, v19 op_sel:[0,0,1]
	v_pk_mul_f32 v[20:21], v[102:103], s[98:99]
	v_pk_mul_f32 v[22:23], v[104:105], s[98:99]
	v_pk_mul_f32 v[24:25], v[98:99], s[98:99]
	v_pk_mul_f32 v[26:27], v[100:101], s[98:99]
	v_exp_f32_e32 v20, v20
	v_exp_f32_e32 v21, v21
	v_exp_f32_e32 v22, v22
	v_exp_f32_e32 v23, v23
	v_exp_f32_e32 v24, v24
	v_exp_f32_e32 v25, v25
	v_exp_f32_e32 v26, v26
	v_exp_f32_e32 v27, v27
	v_pk_fma_f32 v[20:21], v[20:21], s[100:101], s[100:101]
	v_pk_fma_f32 v[22:23], v[22:23], s[100:101], s[100:101]
	v_pk_fma_f32 v[24:25], v[24:25], s[100:101], s[100:101]
	v_pk_fma_f32 v[26:27], v[26:27], s[100:101], s[100:101]
	v_rcp_f32_e32 v20, v20
	v_rcp_f32_e32 v21, v21
	v_rcp_f32_e32 v22, v22
	v_rcp_f32_e32 v23, v23
	v_rcp_f32_e32 v24, v24
	v_rcp_f32_e32 v25, v25
	v_rcp_f32_e32 v26, v26
	v_rcp_f32_e32 v27, v27
	v_pk_mul_f32 v[20:21], v[102:103], v[20:21]
	v_pk_mul_f32 v[22:23], v[104:105], v[22:23]
	v_pk_mul_f32 v[24:25], v[98:99], v[24:25]
	v_pk_mul_f32 v[26:27], v[100:101], v[26:27]
	v_pk_mul_f32 v[20:21], v[20:21], v[70:71]
	v_pk_mul_f32 v[22:23], v[22:23], v[72:73]
	v_pk_mul_f32 v[24:25], v[24:25], v[66:67]
	v_pk_mul_f32 v[26:27], v[26:27], v[68:69]
	v_med3_f32 v20, v20, s69, v246
	v_med3_f32 v21, v21, s69, v246
	v_med3_f32 v22, v22, s69, v246
	v_med3_f32 v23, v23, s69, v246
	v_med3_f32 v24, v24, s69, v246
	v_med3_f32 v25, v25, s69, v246
	v_med3_f32 v26, v26, s69, v246
	v_med3_f32 v27, v27, s69, v246
	v_cvt_pk_fp8_f32 v8, v20, v21
	v_cvt_pk_fp8_f32 v9, v24, v25
	v_cvt_pk_fp8_f32 v8, v22, v23 op_sel:[0,0,1]
	v_cvt_pk_fp8_f32 v9, v26, v27 op_sel:[0,0,1]
	v_or_b32_e32 v10, v5, v243
	v_ashrrev_i32_e32 v11, 31, v10
	v_lshlrev_b64 v[10:11], 11, v[10:11]
	v_lshl_add_u64 v[10:11], s[8:9], 0, v[10:11]
	v_lshl_add_u64 v[10:11], v[10:11], 0, v[2:3]
	v_permlane16_swap_b32_e32 v6, v8
	v_permlane16_swap_b32_e32 v7, v9
	v_lshl_add_u64 v[10:11], v[10:11], 0, v[210:211]
	global_store_dwordx4 v[10:11], v[6:9], off
	s_nop 1
	s_andn2_b64 vcc, exec, s[26:27]
	s_cbranch_vccnz .LBB0_1060
	s_andn2_b64 vcc, exec, s[6:7]
	s_cbranch_vccnz .LBB0_1059
	s_barrier
	s_branch .LBB0_1059
